# attention QK: K-fragment ds_reads pipelined 3 pairs deep (v236-251 as extra buffers) in all 4 QK blocks; on top of pre-claim
# speedup vs baseline: 1.0011x; 1.0011x over previous
.LBB0_709:
	v_add_u32_e32 v3, v219, v220
	ds_read_b128 v[4:7], v3
	ds_read_b128 v[8:11], v3 offset:8192
	v_add_u32_e32 v3, v219, v221
	ds_read_b128 v[236:239], v3
	ds_read_b128 v[240:243], v3 offset:8192
	v_add_u32_e32 v3, v219, v222
	ds_read_b128 v[244:247], v3
	ds_read_b128 v[248:251], v3 offset:8192
	s_add_i32 s27, s25, 0x7f
	s_cmp_lt_i32 s27, s23
	v_add_u32_e32 v3, v219, v223
	s_waitcnt vmcnt(15) lgkmcnt(5)
	v_mfma_f32_32x32x16_bf16 v[82:97], v[4:7], v[114:117], 0
	s_waitcnt lgkmcnt(4)
	v_mfma_f32_32x32x16_bf16 v[98:113], v[8:11], v[114:117], 0
	ds_read_b128 v[4:7], v3
	ds_read_b128 v[8:11], v3 offset:8192
	v_add_u32_e32 v3, v219, v224
	s_waitcnt vmcnt(14) lgkmcnt(5)
	v_mfma_f32_32x32x16_bf16 v[82:97], v[236:239], v[118:121], v[82:97]
	s_waitcnt lgkmcnt(4)
	v_mfma_f32_32x32x16_bf16 v[98:113], v[240:243], v[118:121], v[98:113]
	ds_read_b128 v[236:239], v3
	ds_read_b128 v[240:243], v3 offset:8192
	v_add_u32_e32 v3, v219, v225
	s_waitcnt vmcnt(13) lgkmcnt(5)
	v_mfma_f32_32x32x16_bf16 v[82:97], v[244:247], v[122:125], v[82:97]
	s_waitcnt lgkmcnt(4)
	v_mfma_f32_32x32x16_bf16 v[98:113], v[248:251], v[122:125], v[98:113]
	ds_read_b128 v[244:247], v3
	ds_read_b128 v[248:251], v3 offset:8192
	v_add_u32_e32 v3, v219, v226
	s_waitcnt vmcnt(12) lgkmcnt(5)
	v_mfma_f32_32x32x16_bf16 v[82:97], v[4:7], v[126:129], v[82:97]
	s_waitcnt lgkmcnt(4)
	v_mfma_f32_32x32x16_bf16 v[98:113], v[8:11], v[126:129], v[98:113]
	ds_read_b128 v[4:7], v3
	ds_read_b128 v[8:11], v3 offset:8192
	v_add_u32_e32 v3, v219, v227
	s_waitcnt vmcnt(11) lgkmcnt(5)
	v_mfma_f32_32x32x16_bf16 v[82:97], v[236:239], v[130:133], v[82:97]
	s_waitcnt lgkmcnt(4)
	v_mfma_f32_32x32x16_bf16 v[98:113], v[240:243], v[130:133], v[98:113]
	ds_read_b128 v[236:239], v3
	ds_read_b128 v[240:243], v3 offset:8192
	s_waitcnt vmcnt(10) lgkmcnt(5)
	v_mfma_f32_32x32x16_bf16 v[82:97], v[244:247], v[134:137], v[82:97]
	s_waitcnt lgkmcnt(4)
	v_mfma_f32_32x32x16_bf16 v[98:113], v[248:251], v[134:137], v[98:113]
	s_waitcnt vmcnt(9) lgkmcnt(3)
	v_mfma_f32_32x32x16_bf16 v[82:97], v[4:7], v[138:141], v[82:97]
	s_waitcnt lgkmcnt(2)
	v_mfma_f32_32x32x16_bf16 v[98:113], v[8:11], v[138:141], v[98:113]
	s_waitcnt vmcnt(8) lgkmcnt(1)
	v_mfma_f32_32x32x16_bf16 v[82:97], v[236:239], v[142:145], v[82:97]
	s_waitcnt lgkmcnt(0)
	v_mfma_f32_32x32x16_bf16 v[98:113], v[240:243], v[142:145], v[98:113]
	s_cbranch_scc1 .LBB0_711
	v_add_u32_e32 v3, s25, v217
	v_add_u32_e32 v4, 64, v3
	v_cmp_lt_i32_e32 vcc, v4, v234
	v_add_u32_e32 v4, 0x60, v3
	s_nop 4
	v_cndmask_b32_e32 v82, v233, v82, vcc
	v_cmp_lt_i32_e32 vcc, v4, v234
	v_add_u32_e32 v4, 0x41, v3
	s_nop 0
	v_cndmask_b32_e32 v98, v233, v98, vcc
	v_cmp_lt_i32_e32 vcc, v4, v234
	v_add_u32_e32 v4, 0x61, v3
	s_nop 0
	v_cndmask_b32_e32 v83, v233, v83, vcc
	v_cmp_lt_i32_e32 vcc, v4, v234
	v_add_u32_e32 v4, 0x42, v3
	s_nop 0
	v_cndmask_b32_e32 v99, v233, v99, vcc
	v_cmp_lt_i32_e32 vcc, v4, v234
	v_add_u32_e32 v4, 0x62, v3
	s_nop 0
	v_cndmask_b32_e32 v84, v233, v84, vcc
	v_cmp_lt_i32_e32 vcc, v4, v234
	v_add_u32_e32 v4, 0x43, v3
	s_nop 0
	v_cndmask_b32_e32 v100, v233, v100, vcc
	v_cmp_lt_i32_e32 vcc, v4, v234
	v_add_u32_e32 v4, 0x63, v3
	s_nop 0
	v_cndmask_b32_e32 v85, v233, v85, vcc
	v_cmp_lt_i32_e32 vcc, v4, v234
	v_add_u32_e32 v4, 0x48, v3
	s_nop 0
	v_cndmask_b32_e32 v101, v233, v101, vcc
	v_cmp_lt_i32_e32 vcc, v4, v234
	v_add_u32_e32 v4, 0x68, v3
	s_nop 0
	v_cndmask_b32_e32 v86, v233, v86, vcc
	v_cmp_lt_i32_e32 vcc, v4, v234
	v_add_u32_e32 v4, 0x49, v3
	s_nop 0
	v_cndmask_b32_e32 v102, v233, v102, vcc
	v_cmp_lt_i32_e32 vcc, v4, v234
	v_add_u32_e32 v4, 0x69, v3
	s_nop 0
	v_cndmask_b32_e32 v87, v233, v87, vcc
	v_cmp_lt_i32_e32 vcc, v4, v234
	v_add_u32_e32 v4, 0x4a, v3
	s_nop 0
	v_cndmask_b32_e32 v103, v233, v103, vcc
	v_cmp_lt_i32_e32 vcc, v4, v234
	v_add_u32_e32 v4, 0x6a, v3
	s_nop 0
	v_cndmask_b32_e32 v88, v233, v88, vcc
	v_cmp_lt_i32_e32 vcc, v4, v234
	v_add_u32_e32 v4, 0x4b, v3
	s_nop 0
	v_cndmask_b32_e32 v104, v233, v104, vcc
	v_cmp_lt_i32_e32 vcc, v4, v234
	v_add_u32_e32 v4, 0x6b, v3
	s_nop 0
	v_cndmask_b32_e32 v89, v233, v89, vcc
	v_cmp_lt_i32_e32 vcc, v4, v234
	v_add_u32_e32 v4, 0x50, v3
	s_nop 0
	v_cndmask_b32_e32 v105, v233, v105, vcc
	v_cmp_lt_i32_e32 vcc, v4, v234
	v_add_u32_e32 v4, 0x70, v3
	s_nop 0
	v_cndmask_b32_e32 v90, v233, v90, vcc
	v_cmp_lt_i32_e32 vcc, v4, v234
	v_add_u32_e32 v4, 0x51, v3
	s_nop 0
	v_cndmask_b32_e32 v106, v233, v106, vcc
	v_cmp_lt_i32_e32 vcc, v4, v234
	v_add_u32_e32 v4, 0x71, v3
	s_nop 0
	v_cndmask_b32_e32 v91, v233, v91, vcc
	v_cmp_lt_i32_e32 vcc, v4, v234
	v_add_u32_e32 v4, 0x52, v3
	s_nop 0
	v_cndmask_b32_e32 v107, v233, v107, vcc
	v_cmp_lt_i32_e32 vcc, v4, v234
	v_add_u32_e32 v4, 0x72, v3
	s_nop 0
	v_cndmask_b32_e32 v92, v233, v92, vcc
	v_cmp_lt_i32_e32 vcc, v4, v234
	v_add_u32_e32 v4, 0x53, v3
	s_nop 0
	v_cndmask_b32_e32 v108, v233, v108, vcc
	v_cmp_lt_i32_e32 vcc, v4, v234
	v_add_u32_e32 v4, 0x73, v3
	s_nop 0
	v_cndmask_b32_e32 v93, v233, v93, vcc
	v_cmp_lt_i32_e32 vcc, v4, v234
	v_add_u32_e32 v4, 0x58, v3
	s_nop 0
	v_cndmask_b32_e32 v109, v233, v109, vcc
	v_cmp_lt_i32_e32 vcc, v4, v234
	v_add_u32_e32 v4, 0x78, v3
	s_nop 0
	v_cndmask_b32_e32 v94, v233, v94, vcc
	v_cmp_lt_i32_e32 vcc, v4, v234
	v_add_u32_e32 v4, 0x59, v3
	s_nop 0
	v_cndmask_b32_e32 v110, v233, v110, vcc
	v_cmp_lt_i32_e32 vcc, v4, v234
	v_add_u32_e32 v4, 0x79, v3
	s_nop 0
	v_cndmask_b32_e32 v95, v233, v95, vcc
	v_cmp_lt_i32_e32 vcc, v4, v234
	v_add_u32_e32 v4, 0x5a, v3
	s_nop 0
	v_cndmask_b32_e32 v111, v233, v111, vcc
	v_cmp_lt_i32_e32 vcc, v4, v234
	v_add_u32_e32 v4, 0x7a, v3
	s_nop 0
	v_cndmask_b32_e32 v96, v233, v96, vcc
	v_cmp_lt_i32_e32 vcc, v4, v234
	v_add_u32_e32 v4, 0x5b, v3
	v_add_u32_e32 v3, 0x7b, v3
	v_cndmask_b32_e32 v112, v233, v112, vcc
	v_cmp_lt_i32_e32 vcc, v4, v234
	s_nop 1
	v_cndmask_b32_e32 v97, v233, v97, vcc
	v_cmp_lt_i32_e32 vcc, v3, v234
	s_nop 1
	v_cndmask_b32_e32 v113, v233, v113, vcc

.LBB0_714:
	s_cmp_ge_i32 s25, s24
	s_cbranch_scc1 .LBB0_718
	v_add_u32_e32 v3, v219, v220
	ds_read_b128 v[4:7], v3 offset:16384
	ds_read_b128 v[8:11], v3 offset:24576
	v_add_u32_e32 v3, v219, v221
	ds_read_b128 v[236:239], v3 offset:16384
	ds_read_b128 v[240:243], v3 offset:24576
	v_add_u32_e32 v3, v219, v222
	ds_read_b128 v[244:247], v3 offset:16384
	ds_read_b128 v[248:251], v3 offset:24576
	s_add_i32 s27, s25, 63
	s_cmp_lt_i32 s27, s23
	v_add_u32_e32 v3, v219, v223
	s_waitcnt lgkmcnt(5)
	v_mfma_f32_32x32x16_bf16 v[82:97], v[4:7], v[114:117], 0
	s_waitcnt lgkmcnt(4)
	v_mfma_f32_32x32x16_bf16 v[98:113], v[8:11], v[114:117], 0
	ds_read_b128 v[4:7], v3 offset:16384
	ds_read_b128 v[8:11], v3 offset:24576
	v_add_u32_e32 v3, v219, v224
	s_waitcnt lgkmcnt(5)
	v_mfma_f32_32x32x16_bf16 v[82:97], v[236:239], v[118:121], v[82:97]
	s_waitcnt lgkmcnt(4)
	v_mfma_f32_32x32x16_bf16 v[98:113], v[240:243], v[118:121], v[98:113]
	ds_read_b128 v[236:239], v3 offset:16384
	ds_read_b128 v[240:243], v3 offset:24576
	v_add_u32_e32 v3, v219, v225
	s_waitcnt lgkmcnt(5)
	v_mfma_f32_32x32x16_bf16 v[82:97], v[244:247], v[122:125], v[82:97]
	s_waitcnt lgkmcnt(4)
	v_mfma_f32_32x32x16_bf16 v[98:113], v[248:251], v[122:125], v[98:113]
	ds_read_b128 v[244:247], v3 offset:16384
	ds_read_b128 v[248:251], v3 offset:24576
	v_add_u32_e32 v3, v219, v226
	s_waitcnt lgkmcnt(5)
	v_mfma_f32_32x32x16_bf16 v[82:97], v[4:7], v[126:129], v[82:97]
	s_waitcnt lgkmcnt(4)
	v_mfma_f32_32x32x16_bf16 v[98:113], v[8:11], v[126:129], v[98:113]
	ds_read_b128 v[4:7], v3 offset:16384
	ds_read_b128 v[8:11], v3 offset:24576
	v_add_u32_e32 v3, v219, v227
	s_waitcnt lgkmcnt(5)
	v_mfma_f32_32x32x16_bf16 v[82:97], v[236:239], v[130:133], v[82:97]
	s_waitcnt lgkmcnt(4)
	v_mfma_f32_32x32x16_bf16 v[98:113], v[240:243], v[130:133], v[98:113]
	ds_read_b128 v[236:239], v3 offset:16384
	ds_read_b128 v[240:243], v3 offset:24576
	s_waitcnt lgkmcnt(5)
	v_mfma_f32_32x32x16_bf16 v[82:97], v[244:247], v[134:137], v[82:97]
	s_waitcnt lgkmcnt(4)
	v_mfma_f32_32x32x16_bf16 v[98:113], v[248:251], v[134:137], v[98:113]
	s_waitcnt lgkmcnt(3)
	v_mfma_f32_32x32x16_bf16 v[82:97], v[4:7], v[138:141], v[82:97]
	s_waitcnt lgkmcnt(2)
	v_mfma_f32_32x32x16_bf16 v[98:113], v[8:11], v[138:141], v[98:113]
	s_waitcnt lgkmcnt(1)
	v_mfma_f32_32x32x16_bf16 v[82:97], v[236:239], v[142:145], v[82:97]
	s_waitcnt lgkmcnt(0)
	v_mfma_f32_32x32x16_bf16 v[98:113], v[240:243], v[142:145], v[98:113]
	s_cbranch_scc1 .LBB0_717
	v_add_u32_e32 v3, s25, v217
	v_cmp_lt_i32_e32 vcc, v3, v234
	v_add_u32_e32 v4, 32, v3
	s_nop 5
	v_cndmask_b32_e32 v82, v233, v82, vcc
	v_cmp_lt_i32_e32 vcc, v4, v234
	v_add_u32_e32 v4, 1, v3
	s_nop 0
	v_cndmask_b32_e32 v98, v233, v98, vcc
	v_cmp_lt_i32_e32 vcc, v4, v234
	v_add_u32_e32 v4, 33, v3
	s_nop 0
	v_cndmask_b32_e32 v83, v233, v83, vcc
	v_cmp_lt_i32_e32 vcc, v4, v234
	v_add_u32_e32 v4, 2, v3
	s_nop 0
	v_cndmask_b32_e32 v99, v233, v99, vcc
	v_cmp_lt_i32_e32 vcc, v4, v234
	v_add_u32_e32 v4, 34, v3
	s_nop 0
	v_cndmask_b32_e32 v84, v233, v84, vcc
	v_cmp_lt_i32_e32 vcc, v4, v234
	v_add_u32_e32 v4, 3, v3
	s_nop 0
	v_cndmask_b32_e32 v100, v233, v100, vcc
	v_cmp_lt_i32_e32 vcc, v4, v234
	v_add_u32_e32 v4, 35, v3
	s_nop 0
	v_cndmask_b32_e32 v85, v233, v85, vcc
	v_cmp_lt_i32_e32 vcc, v4, v234
	v_add_u32_e32 v4, 8, v3
	s_nop 0
	v_cndmask_b32_e32 v101, v233, v101, vcc
	v_cmp_lt_i32_e32 vcc, v4, v234
	v_add_u32_e32 v4, 40, v3
	s_nop 0
	v_cndmask_b32_e32 v86, v233, v86, vcc
	v_cmp_lt_i32_e32 vcc, v4, v234
	v_add_u32_e32 v4, 9, v3
	s_nop 0
	v_cndmask_b32_e32 v102, v233, v102, vcc
	v_cmp_lt_i32_e32 vcc, v4, v234
	v_add_u32_e32 v4, 41, v3
	s_nop 0
	v_cndmask_b32_e32 v87, v233, v87, vcc
	v_cmp_lt_i32_e32 vcc, v4, v234
	v_add_u32_e32 v4, 10, v3
	s_nop 0
	v_cndmask_b32_e32 v103, v233, v103, vcc
	v_cmp_lt_i32_e32 vcc, v4, v234
	v_add_u32_e32 v4, 42, v3
	s_nop 0
	v_cndmask_b32_e32 v88, v233, v88, vcc
	v_cmp_lt_i32_e32 vcc, v4, v234
	v_add_u32_e32 v4, 11, v3
	s_nop 0
	v_cndmask_b32_e32 v104, v233, v104, vcc
	v_cmp_lt_i32_e32 vcc, v4, v234
	v_add_u32_e32 v4, 43, v3
	s_nop 0
	v_cndmask_b32_e32 v89, v233, v89, vcc
	v_cmp_lt_i32_e32 vcc, v4, v234
	v_add_u32_e32 v4, 16, v3
	s_nop 0
	v_cndmask_b32_e32 v105, v233, v105, vcc
	v_cmp_lt_i32_e32 vcc, v4, v234
	v_add_u32_e32 v4, 48, v3
	s_nop 0
	v_cndmask_b32_e32 v90, v233, v90, vcc
	v_cmp_lt_i32_e32 vcc, v4, v234
	v_add_u32_e32 v4, 17, v3
	s_nop 0
	v_cndmask_b32_e32 v106, v233, v106, vcc
	v_cmp_lt_i32_e32 vcc, v4, v234
	v_add_u32_e32 v4, 49, v3
	s_nop 0
	v_cndmask_b32_e32 v91, v233, v91, vcc
	v_cmp_lt_i32_e32 vcc, v4, v234
	v_add_u32_e32 v4, 18, v3
	s_nop 0
	v_cndmask_b32_e32 v107, v233, v107, vcc
	v_cmp_lt_i32_e32 vcc, v4, v234
	v_add_u32_e32 v4, 50, v3
	s_nop 0
	v_cndmask_b32_e32 v92, v233, v92, vcc
	v_cmp_lt_i32_e32 vcc, v4, v234
	v_add_u32_e32 v4, 19, v3
	s_nop 0
	v_cndmask_b32_e32 v108, v233, v108, vcc
	v_cmp_lt_i32_e32 vcc, v4, v234
	v_add_u32_e32 v4, 51, v3
	s_nop 0
	v_cndmask_b32_e32 v93, v233, v93, vcc
	v_cmp_lt_i32_e32 vcc, v4, v234
	v_add_u32_e32 v4, 24, v3
	s_nop 0
	v_cndmask_b32_e32 v109, v233, v109, vcc
	v_cmp_lt_i32_e32 vcc, v4, v234
	v_add_u32_e32 v4, 56, v3
	s_nop 0
	v_cndmask_b32_e32 v94, v233, v94, vcc
	v_cmp_lt_i32_e32 vcc, v4, v234
	v_add_u32_e32 v4, 25, v3
	s_nop 0
	v_cndmask_b32_e32 v110, v233, v110, vcc
	v_cmp_lt_i32_e32 vcc, v4, v234
	v_add_u32_e32 v4, 57, v3
	s_nop 0
	v_cndmask_b32_e32 v95, v233, v95, vcc
	v_cmp_lt_i32_e32 vcc, v4, v234
	v_add_u32_e32 v4, 26, v3
	s_nop 0
	v_cndmask_b32_e32 v111, v233, v111, vcc
	v_cmp_lt_i32_e32 vcc, v4, v234
	v_add_u32_e32 v4, 58, v3
	s_nop 0
	v_cndmask_b32_e32 v96, v233, v96, vcc
	v_cmp_lt_i32_e32 vcc, v4, v234
	v_add_u32_e32 v4, 27, v3
	v_add_u32_e32 v3, 59, v3
	v_cndmask_b32_e32 v112, v233, v112, vcc
	v_cmp_lt_i32_e32 vcc, v4, v234
	s_nop 1
	v_cndmask_b32_e32 v97, v233, v97, vcc
	v_cmp_lt_i32_e32 vcc, v3, v234
	s_nop 1
	v_cndmask_b32_e32 v113, v233, v113, vcc

.LBB0_2277:
	v_add_u32_e32 v3, v219, v220
	ds_read_b128 v[4:7], v3
	ds_read_b128 v[8:11], v3 offset:8192
	v_add_u32_e32 v3, v219, v221
	ds_read_b128 v[236:239], v3
	ds_read_b128 v[240:243], v3 offset:8192
	v_add_u32_e32 v3, v219, v222
	ds_read_b128 v[244:247], v3
	ds_read_b128 v[248:251], v3 offset:8192
	s_add_i32 s26, s31, 0x7f
	s_cmp_lt_i32 s26, s29
	v_add_u32_e32 v3, v219, v223
	s_waitcnt vmcnt(15) lgkmcnt(5)
	v_mfma_f32_32x32x16_bf16 v[82:97], v[4:7], v[114:117], 0
	s_waitcnt lgkmcnt(4)
	v_mfma_f32_32x32x16_bf16 v[98:113], v[8:11], v[114:117], 0
	ds_read_b128 v[4:7], v3
	ds_read_b128 v[8:11], v3 offset:8192
	v_add_u32_e32 v3, v219, v224
	s_waitcnt vmcnt(14) lgkmcnt(5)
	v_mfma_f32_32x32x16_bf16 v[82:97], v[236:239], v[118:121], v[82:97]
	s_waitcnt lgkmcnt(4)
	v_mfma_f32_32x32x16_bf16 v[98:113], v[240:243], v[118:121], v[98:113]
	ds_read_b128 v[236:239], v3
	ds_read_b128 v[240:243], v3 offset:8192
	v_add_u32_e32 v3, v219, v225
	s_waitcnt vmcnt(13) lgkmcnt(5)
	v_mfma_f32_32x32x16_bf16 v[82:97], v[244:247], v[122:125], v[82:97]
	s_waitcnt lgkmcnt(4)
	v_mfma_f32_32x32x16_bf16 v[98:113], v[248:251], v[122:125], v[98:113]
	ds_read_b128 v[244:247], v3
	ds_read_b128 v[248:251], v3 offset:8192
	v_add_u32_e32 v3, v219, v226
	s_waitcnt vmcnt(12) lgkmcnt(5)
	v_mfma_f32_32x32x16_bf16 v[82:97], v[4:7], v[126:129], v[82:97]
	s_waitcnt lgkmcnt(4)
	v_mfma_f32_32x32x16_bf16 v[98:113], v[8:11], v[126:129], v[98:113]
	ds_read_b128 v[4:7], v3
	ds_read_b128 v[8:11], v3 offset:8192
	v_add_u32_e32 v3, v219, v227
	s_waitcnt vmcnt(11) lgkmcnt(5)
	v_mfma_f32_32x32x16_bf16 v[82:97], v[236:239], v[130:133], v[82:97]
	s_waitcnt lgkmcnt(4)
	v_mfma_f32_32x32x16_bf16 v[98:113], v[240:243], v[130:133], v[98:113]
	ds_read_b128 v[236:239], v3
	ds_read_b128 v[240:243], v3 offset:8192
	s_waitcnt vmcnt(10) lgkmcnt(5)
	v_mfma_f32_32x32x16_bf16 v[82:97], v[244:247], v[134:137], v[82:97]
	s_waitcnt lgkmcnt(4)
	v_mfma_f32_32x32x16_bf16 v[98:113], v[248:251], v[134:137], v[98:113]
	s_waitcnt vmcnt(9) lgkmcnt(3)
	v_mfma_f32_32x32x16_bf16 v[82:97], v[4:7], v[138:141], v[82:97]
	s_waitcnt lgkmcnt(2)
	v_mfma_f32_32x32x16_bf16 v[98:113], v[8:11], v[138:141], v[98:113]
	s_waitcnt vmcnt(8) lgkmcnt(1)
	v_mfma_f32_32x32x16_bf16 v[82:97], v[236:239], v[142:145], v[82:97]
	s_waitcnt lgkmcnt(0)
	v_mfma_f32_32x32x16_bf16 v[98:113], v[240:243], v[142:145], v[98:113]
	s_cbranch_scc1 .LBB0_2279
	v_add_u32_e32 v3, s31, v217
	v_add_u32_e32 v4, 64, v3
	v_cmp_lt_i32_e32 vcc, v4, v234
	v_add_u32_e32 v4, 0x60, v3
	s_nop 4
	v_cndmask_b32_e32 v82, v233, v82, vcc
	v_cmp_lt_i32_e32 vcc, v4, v234
	v_add_u32_e32 v4, 0x41, v3
	s_nop 0
	v_cndmask_b32_e32 v98, v233, v98, vcc
	v_cmp_lt_i32_e32 vcc, v4, v234
	v_add_u32_e32 v4, 0x61, v3
	s_nop 0
	v_cndmask_b32_e32 v83, v233, v83, vcc
	v_cmp_lt_i32_e32 vcc, v4, v234
	v_add_u32_e32 v4, 0x42, v3
	s_nop 0
	v_cndmask_b32_e32 v99, v233, v99, vcc
	v_cmp_lt_i32_e32 vcc, v4, v234
	v_add_u32_e32 v4, 0x62, v3
	s_nop 0
	v_cndmask_b32_e32 v84, v233, v84, vcc
	v_cmp_lt_i32_e32 vcc, v4, v234
	v_add_u32_e32 v4, 0x43, v3
	s_nop 0
	v_cndmask_b32_e32 v100, v233, v100, vcc
	v_cmp_lt_i32_e32 vcc, v4, v234
	v_add_u32_e32 v4, 0x63, v3
	s_nop 0
	v_cndmask_b32_e32 v85, v233, v85, vcc
	v_cmp_lt_i32_e32 vcc, v4, v234
	v_add_u32_e32 v4, 0x48, v3
	s_nop 0
	v_cndmask_b32_e32 v101, v233, v101, vcc
	v_cmp_lt_i32_e32 vcc, v4, v234
	v_add_u32_e32 v4, 0x68, v3
	s_nop 0
	v_cndmask_b32_e32 v86, v233, v86, vcc
	v_cmp_lt_i32_e32 vcc, v4, v234
	v_add_u32_e32 v4, 0x49, v3
	s_nop 0
	v_cndmask_b32_e32 v102, v233, v102, vcc
	v_cmp_lt_i32_e32 vcc, v4, v234
	v_add_u32_e32 v4, 0x69, v3
	s_nop 0
	v_cndmask_b32_e32 v87, v233, v87, vcc
	v_cmp_lt_i32_e32 vcc, v4, v234
	v_add_u32_e32 v4, 0x4a, v3
	s_nop 0
	v_cndmask_b32_e32 v103, v233, v103, vcc
	v_cmp_lt_i32_e32 vcc, v4, v234
	v_add_u32_e32 v4, 0x6a, v3
	s_nop 0
	v_cndmask_b32_e32 v88, v233, v88, vcc
	v_cmp_lt_i32_e32 vcc, v4, v234
	v_add_u32_e32 v4, 0x4b, v3
	s_nop 0
	v_cndmask_b32_e32 v104, v233, v104, vcc
	v_cmp_lt_i32_e32 vcc, v4, v234
	v_add_u32_e32 v4, 0x6b, v3
	s_nop 0
	v_cndmask_b32_e32 v89, v233, v89, vcc
	v_cmp_lt_i32_e32 vcc, v4, v234
	v_add_u32_e32 v4, 0x50, v3
	s_nop 0
	v_cndmask_b32_e32 v105, v233, v105, vcc
	v_cmp_lt_i32_e32 vcc, v4, v234
	v_add_u32_e32 v4, 0x70, v3
	s_nop 0
	v_cndmask_b32_e32 v90, v233, v90, vcc
	v_cmp_lt_i32_e32 vcc, v4, v234
	v_add_u32_e32 v4, 0x51, v3
	s_nop 0
	v_cndmask_b32_e32 v106, v233, v106, vcc
	v_cmp_lt_i32_e32 vcc, v4, v234
	v_add_u32_e32 v4, 0x71, v3
	s_nop 0
	v_cndmask_b32_e32 v91, v233, v91, vcc
	v_cmp_lt_i32_e32 vcc, v4, v234
	v_add_u32_e32 v4, 0x52, v3
	s_nop 0
	v_cndmask_b32_e32 v107, v233, v107, vcc
	v_cmp_lt_i32_e32 vcc, v4, v234
	v_add_u32_e32 v4, 0x72, v3
	s_nop 0
	v_cndmask_b32_e32 v92, v233, v92, vcc
	v_cmp_lt_i32_e32 vcc, v4, v234
	v_add_u32_e32 v4, 0x53, v3
	s_nop 0
	v_cndmask_b32_e32 v108, v233, v108, vcc
	v_cmp_lt_i32_e32 vcc, v4, v234
	v_add_u32_e32 v4, 0x73, v3
	s_nop 0
	v_cndmask_b32_e32 v93, v233, v93, vcc
	v_cmp_lt_i32_e32 vcc, v4, v234
	v_add_u32_e32 v4, 0x58, v3
	s_nop 0
	v_cndmask_b32_e32 v109, v233, v109, vcc
	v_cmp_lt_i32_e32 vcc, v4, v234
	v_add_u32_e32 v4, 0x78, v3
	s_nop 0
	v_cndmask_b32_e32 v94, v233, v94, vcc
	v_cmp_lt_i32_e32 vcc, v4, v234
	v_add_u32_e32 v4, 0x59, v3
	s_nop 0
	v_cndmask_b32_e32 v110, v233, v110, vcc
	v_cmp_lt_i32_e32 vcc, v4, v234
	v_add_u32_e32 v4, 0x79, v3
	s_nop 0
	v_cndmask_b32_e32 v95, v233, v95, vcc
	v_cmp_lt_i32_e32 vcc, v4, v234
	v_add_u32_e32 v4, 0x5a, v3
	s_nop 0
	v_cndmask_b32_e32 v111, v233, v111, vcc
	v_cmp_lt_i32_e32 vcc, v4, v234
	v_add_u32_e32 v4, 0x7a, v3
	s_nop 0
	v_cndmask_b32_e32 v96, v233, v96, vcc
	v_cmp_lt_i32_e32 vcc, v4, v234
	v_add_u32_e32 v4, 0x5b, v3
	v_add_u32_e32 v3, 0x7b, v3
	v_cndmask_b32_e32 v112, v233, v112, vcc
	v_cmp_lt_i32_e32 vcc, v4, v234
	s_nop 1
	v_cndmask_b32_e32 v97, v233, v97, vcc
	v_cmp_lt_i32_e32 vcc, v3, v234
	s_nop 1
	v_cndmask_b32_e32 v113, v233, v113, vcc

.LBB0_2282:
	s_cmp_ge_i32 s31, s30
	s_cbranch_scc1 .LBB0_2286
	v_add_u32_e32 v3, v219, v220
	ds_read_b128 v[4:7], v3 offset:16384
	ds_read_b128 v[8:11], v3 offset:24576
	v_add_u32_e32 v3, v219, v221
	ds_read_b128 v[236:239], v3 offset:16384
	ds_read_b128 v[240:243], v3 offset:24576
	v_add_u32_e32 v3, v219, v222
	ds_read_b128 v[244:247], v3 offset:16384
	ds_read_b128 v[248:251], v3 offset:24576
	s_add_i32 s26, s31, 63
	s_cmp_lt_i32 s26, s29
	v_add_u32_e32 v3, v219, v223
	s_waitcnt lgkmcnt(5)
	v_mfma_f32_32x32x16_bf16 v[82:97], v[4:7], v[114:117], 0
	s_waitcnt lgkmcnt(4)
	v_mfma_f32_32x32x16_bf16 v[98:113], v[8:11], v[114:117], 0
	ds_read_b128 v[4:7], v3 offset:16384
	ds_read_b128 v[8:11], v3 offset:24576
	v_add_u32_e32 v3, v219, v224
	s_waitcnt lgkmcnt(5)
	v_mfma_f32_32x32x16_bf16 v[82:97], v[236:239], v[118:121], v[82:97]
	s_waitcnt lgkmcnt(4)
	v_mfma_f32_32x32x16_bf16 v[98:113], v[240:243], v[118:121], v[98:113]
	ds_read_b128 v[236:239], v3 offset:16384
	ds_read_b128 v[240:243], v3 offset:24576
	v_add_u32_e32 v3, v219, v225
	s_waitcnt lgkmcnt(5)
	v_mfma_f32_32x32x16_bf16 v[82:97], v[244:247], v[122:125], v[82:97]
	s_waitcnt lgkmcnt(4)
	v_mfma_f32_32x32x16_bf16 v[98:113], v[248:251], v[122:125], v[98:113]
	ds_read_b128 v[244:247], v3 offset:16384
	ds_read_b128 v[248:251], v3 offset:24576
	v_add_u32_e32 v3, v219, v226
	s_waitcnt lgkmcnt(5)
	v_mfma_f32_32x32x16_bf16 v[82:97], v[4:7], v[126:129], v[82:97]
	s_waitcnt lgkmcnt(4)
	v_mfma_f32_32x32x16_bf16 v[98:113], v[8:11], v[126:129], v[98:113]
	ds_read_b128 v[4:7], v3 offset:16384
	ds_read_b128 v[8:11], v3 offset:24576
	v_add_u32_e32 v3, v219, v227
	s_waitcnt lgkmcnt(5)
	v_mfma_f32_32x32x16_bf16 v[82:97], v[236:239], v[130:133], v[82:97]
	s_waitcnt lgkmcnt(4)
	v_mfma_f32_32x32x16_bf16 v[98:113], v[240:243], v[130:133], v[98:113]
	ds_read_b128 v[236:239], v3 offset:16384
	ds_read_b128 v[240:243], v3 offset:24576
	s_waitcnt lgkmcnt(5)
	v_mfma_f32_32x32x16_bf16 v[82:97], v[244:247], v[134:137], v[82:97]
	s_waitcnt lgkmcnt(4)
	v_mfma_f32_32x32x16_bf16 v[98:113], v[248:251], v[134:137], v[98:113]
	s_waitcnt lgkmcnt(3)
	v_mfma_f32_32x32x16_bf16 v[82:97], v[4:7], v[138:141], v[82:97]
	s_waitcnt lgkmcnt(2)
	v_mfma_f32_32x32x16_bf16 v[98:113], v[8:11], v[138:141], v[98:113]
	s_waitcnt lgkmcnt(1)
	v_mfma_f32_32x32x16_bf16 v[82:97], v[236:239], v[142:145], v[82:97]
	s_waitcnt lgkmcnt(0)
	v_mfma_f32_32x32x16_bf16 v[98:113], v[240:243], v[142:145], v[98:113]
	s_cbranch_scc1 .LBB0_2285
	v_add_u32_e32 v3, s31, v217
	v_cmp_lt_i32_e32 vcc, v3, v234
	v_add_u32_e32 v4, 32, v3
	s_nop 5
	v_cndmask_b32_e32 v82, v233, v82, vcc
	v_cmp_lt_i32_e32 vcc, v4, v234
	v_add_u32_e32 v4, 1, v3
	s_nop 0
	v_cndmask_b32_e32 v98, v233, v98, vcc
	v_cmp_lt_i32_e32 vcc, v4, v234
	v_add_u32_e32 v4, 33, v3
	s_nop 0
	v_cndmask_b32_e32 v83, v233, v83, vcc
	v_cmp_lt_i32_e32 vcc, v4, v234
	v_add_u32_e32 v4, 2, v3
	s_nop 0
	v_cndmask_b32_e32 v99, v233, v99, vcc
	v_cmp_lt_i32_e32 vcc, v4, v234
	v_add_u32_e32 v4, 34, v3
	s_nop 0
	v_cndmask_b32_e32 v84, v233, v84, vcc
	v_cmp_lt_i32_e32 vcc, v4, v234
	v_add_u32_e32 v4, 3, v3
	s_nop 0
	v_cndmask_b32_e32 v100, v233, v100, vcc
	v_cmp_lt_i32_e32 vcc, v4, v234
	v_add_u32_e32 v4, 35, v3
	s_nop 0
	v_cndmask_b32_e32 v85, v233, v85, vcc
	v_cmp_lt_i32_e32 vcc, v4, v234
	v_add_u32_e32 v4, 8, v3
	s_nop 0
	v_cndmask_b32_e32 v101, v233, v101, vcc
	v_cmp_lt_i32_e32 vcc, v4, v234
	v_add_u32_e32 v4, 40, v3
	s_nop 0
	v_cndmask_b32_e32 v86, v233, v86, vcc
	v_cmp_lt_i32_e32 vcc, v4, v234
	v_add_u32_e32 v4, 9, v3
	s_nop 0
	v_cndmask_b32_e32 v102, v233, v102, vcc
	v_cmp_lt_i32_e32 vcc, v4, v234
	v_add_u32_e32 v4, 41, v3
	s_nop 0
	v_cndmask_b32_e32 v87, v233, v87, vcc
	v_cmp_lt_i32_e32 vcc, v4, v234
	v_add_u32_e32 v4, 10, v3
	s_nop 0
	v_cndmask_b32_e32 v103, v233, v103, vcc
	v_cmp_lt_i32_e32 vcc, v4, v234
	v_add_u32_e32 v4, 42, v3
	s_nop 0
	v_cndmask_b32_e32 v88, v233, v88, vcc
	v_cmp_lt_i32_e32 vcc, v4, v234
	v_add_u32_e32 v4, 11, v3
	s_nop 0
	v_cndmask_b32_e32 v104, v233, v104, vcc
	v_cmp_lt_i32_e32 vcc, v4, v234
	v_add_u32_e32 v4, 43, v3
	s_nop 0
	v_cndmask_b32_e32 v89, v233, v89, vcc
	v_cmp_lt_i32_e32 vcc, v4, v234
	v_add_u32_e32 v4, 16, v3
	s_nop 0
	v_cndmask_b32_e32 v105, v233, v105, vcc
	v_cmp_lt_i32_e32 vcc, v4, v234
	v_add_u32_e32 v4, 48, v3
	s_nop 0
	v_cndmask_b32_e32 v90, v233, v90, vcc
	v_cmp_lt_i32_e32 vcc, v4, v234
	v_add_u32_e32 v4, 17, v3
	s_nop 0
	v_cndmask_b32_e32 v106, v233, v106, vcc
	v_cmp_lt_i32_e32 vcc, v4, v234
	v_add_u32_e32 v4, 49, v3
	s_nop 0
	v_cndmask_b32_e32 v91, v233, v91, vcc
	v_cmp_lt_i32_e32 vcc, v4, v234
	v_add_u32_e32 v4, 18, v3
	s_nop 0
	v_cndmask_b32_e32 v107, v233, v107, vcc
	v_cmp_lt_i32_e32 vcc, v4, v234
	v_add_u32_e32 v4, 50, v3
	s_nop 0
	v_cndmask_b32_e32 v92, v233, v92, vcc
	v_cmp_lt_i32_e32 vcc, v4, v234
	v_add_u32_e32 v4, 19, v3
	s_nop 0
	v_cndmask_b32_e32 v108, v233, v108, vcc
	v_cmp_lt_i32_e32 vcc, v4, v234
	v_add_u32_e32 v4, 51, v3
	s_nop 0
	v_cndmask_b32_e32 v93, v233, v93, vcc
	v_cmp_lt_i32_e32 vcc, v4, v234
	v_add_u32_e32 v4, 24, v3
	s_nop 0
	v_cndmask_b32_e32 v109, v233, v109, vcc
	v_cmp_lt_i32_e32 vcc, v4, v234
	v_add_u32_e32 v4, 56, v3
	s_nop 0
	v_cndmask_b32_e32 v94, v233, v94, vcc
	v_cmp_lt_i32_e32 vcc, v4, v234
	v_add_u32_e32 v4, 25, v3
	s_nop 0
	v_cndmask_b32_e32 v110, v233, v110, vcc
	v_cmp_lt_i32_e32 vcc, v4, v234
	v_add_u32_e32 v4, 57, v3
	s_nop 0
	v_cndmask_b32_e32 v95, v233, v95, vcc
	v_cmp_lt_i32_e32 vcc, v4, v234
	v_add_u32_e32 v4, 26, v3
	s_nop 0
	v_cndmask_b32_e32 v111, v233, v111, vcc
	v_cmp_lt_i32_e32 vcc, v4, v234
	v_add_u32_e32 v4, 58, v3
	s_nop 0
	v_cndmask_b32_e32 v96, v233, v96, vcc
	v_cmp_lt_i32_e32 vcc, v4, v234
	v_add_u32_e32 v4, 27, v3
	v_add_u32_e32 v3, 59, v3
	v_cndmask_b32_e32 v112, v233, v112, vcc
	v_cmp_lt_i32_e32 vcc, v4, v234
	s_nop 1
	v_cndmask_b32_e32 v97, v233, v97, vcc
	v_cmp_lt_i32_e32 vcc, v3, v234
	s_nop 1
	v_cndmask_b32_e32 v113, v233, v113, vcc
